# baseline (speedup 1.0000x reference)
.Lkb_p1_b_end:
.LBB1_14:
	s_mov_b64 exec, -1
	v_cmp_gt_u32_e64 s[4:5], 64, v0
	s_waitcnt lgkmcnt(0)
	s_barrier
	s_and_saveexec_b64 s[6:7], s[4:5]
	s_cbranch_execz .LBB1_16
	v_lshlrev_b32_e32 v10, 3, v0
	ds_read_b64 v[6:7], v10 offset:6176
	s_waitcnt lgkmcnt(0)
	v_add_u32_e32 v7, v7, v6
	v_mov_b32_e32 v8, v7
	s_nop 1
	v_add_u32_dpp v8, v8, v8 row_shr:1 row_mask:0xf bank_mask:0xf
	s_nop 1
	v_add_u32_dpp v8, v8, v8 row_shr:2 row_mask:0xf bank_mask:0xf
	s_nop 1
	v_add_u32_dpp v8, v8, v8 row_shr:4 row_mask:0xf bank_mask:0xf
	s_nop 1
	v_add_u32_dpp v8, v8, v8 row_shr:8 row_mask:0xf bank_mask:0xf
	s_nop 1
	v_add_u32_dpp v8, v8, v8 row_bcast:15 row_mask:0xa bank_mask:0xf
	s_nop 1
	v_add_u32_dpp v8, v8, v8 row_bcast:31 row_mask:0xc bank_mask:0xf
	v_sub_u32_e32 v8, v8, v7
	v_add_u32_e32 v9, v8, v6
	ds_write_b64 v10, v[8:9] offset:6688

.LBB1_32:
	s_endpgm
	s_nop 0
	s_nop 0
	s_nop 0
	s_nop 0
	s_nop 0
	s_nop 0
	s_nop 0
	s_nop 0
	s_nop 0
	s_nop 0
	s_nop 0
	s_nop 0
	s_nop 0
	s_nop 0
	s_nop 0
	s_nop 0
	s_nop 0
	s_nop 0
	s_nop 0
	s_nop 0
	s_nop 0
	s_nop 0
	s_nop 0
	s_nop 0
	s_nop 0
	s_nop 0
	s_nop 0
	s_nop 0
	s_nop 0
	s_nop 0
	s_nop 0
	s_nop 0
	s_nop 0
	s_nop 0
	s_nop 0
	s_nop 0
	s_nop 0
	s_nop 0
	s_nop 0
	s_nop 0
	s_nop 0
	s_nop 0
	s_nop 0
	s_nop 0
	s_nop 0
	s_nop 0
	s_nop 0
	s_nop 0
	s_nop 0
	s_nop 0
	s_nop 0
	s_nop 0
	s_nop 0
	s_nop 0
	s_endpgm
